# speedup vs baseline: 1.0006x; 1.0006x over previous
_Z11gemm_kernelILi256ELi192ELi4ELi2ELi4ELi2ELi2ELi0EEvPKDF16_S1_iiiPDF16_PfPK15HIP_vector_typeIfLj2EE:
	s_load_dwordx8 s[4:11], s[0:1], 0x0
	s_load_dwordx2 s[12:13], s[0:1], 0x30
	s_lshr_b32 s18, s2, 3
	v_readfirstlane_b32 s17, v0
	s_lshr_b32 s14, s17, 6
	s_waitcnt lgkmcnt(0)
	s_ashr_i32 s11, s8, 31
	s_lshr_b32 s3, s11, 22
	s_add_i32 s3, s8, s3
	s_ashr_i32 s15, s3, 10
	s_abs_i32 s16, s15
	v_cvt_f32_u32_e32 v1, s16
	s_sub_i32 s21, 0, s16
	s_mul_hi_i32 s19, s9, 0x2aaaaaab
	s_lshr_b32 s20, s19, 31
	v_rcp_iflag_f32_e32 v1, v1
	s_ashr_i32 s19, s19, 6
	s_add_i32 s19, s19, s20
	s_bfe_u32 s20, s2, 0x20001
	v_mul_f32_e32 v1, 0x4f7ffffe, v1
	v_cvt_u32_f32_e32 v1, v1
	s_ashr_i32 s3, s3, 31
	s_mul_i32 s20, s15, s20
	v_mov_b32_e32 v97, 0
	v_readfirstlane_b32 s22, v1
	s_mul_i32 s21, s21, s22
	s_mul_hi_u32 s21, s22, s21
	s_add_i32 s22, s22, s21
	s_mul_hi_u32 s22, s18, s22
	s_mul_i32 s21, s22, s16
	s_sub_i32 s23, s18, s21
	s_add_i32 s24, s22, 1
	s_sub_i32 s25, s23, s16
	s_cmp_ge_u32 s23, s16
	s_cselect_b32 s22, s24, s22
	s_cselect_b32 s23, s25, s23
	s_add_i32 s24, s22, 1
	s_cmp_ge_u32 s23, s16
	s_cselect_b32 s16, s24, s22
	s_xor_b32 s16, s16, s3
	s_sub_i32 s3, s16, s3
	s_mul_i32 s15, s3, s15
	s_sub_i32 s15, s18, s15
	s_add_i32 s15, s15, s20
	s_bitcmp1_b32 s2, 0
	v_bfe_u32 v1, v0, 3, 3
	s_cselect_b32 s2, s19, 0
	v_lshl_or_b32 v1, s14, 3, v1
	s_add_i32 s18, s3, s2
	s_lshl_b32 s19, s15, 8
	v_lshrrev_b32_e32 v2, 1, v1
	s_lshl_b32 s2, s14, 10
	v_xor_b32_e32 v6, v2, v0
	v_add_u32_e32 v2, s19, v1
	s_cmp_lg_u32 0, -1
	s_mul_i32 s15, s18, 0xc0
	v_ashrrev_i32_e32 v3, 31, v2
	s_cselect_b32 s3, 0, 0
	v_lshlrev_b64 v[2:3], 7, v[2:3]
	v_add_u32_e32 v4, s15, v1
	s_add_i32 s22, s2, s3
	v_lshlrev_b32_e32 v1, 4, v6
	s_lshr_b32 s3, s17, 1
	v_lshl_add_u64 v[2:3], s[4:5], 0, v[2:3]
	v_ashrrev_i32_e32 v5, 31, v4
	v_and_b32_e32 v96, 0x70, v1
	s_add_i32 s24, s22, 0x8000
	s_and_b32 s20, s3, 0x7fffffc0
	v_lshlrev_b64 v[4:5], 7, v[4:5]
	v_lshl_add_u64 v[104:105], v[2:3], 0, v[96:97]
	s_bitcmp1_b32 s17, 6
	s_mov_b64 s[4:5], 0x2000
	s_mov_b32 m0, s22
	s_nop 0
	global_load_lds_dwordx4 v[104:105], off
	v_lshl_add_u64 v[4:5], s[6:7], 0, v[4:5]
	s_cselect_b32 s16, 0x60, 0
	v_lshl_add_u64 v[110:111], v[104:105], 0, s[4:5]
	s_mov_b64 s[6:7], 0x4000
	s_add_i32 s3, s22, 0x2000
	s_mov_b32 m0, s3
	s_nop 0
	global_load_lds_dwordx4 v[110:111], off
	v_lshl_add_u64 v[108:109], v[104:105], 0, s[6:7]
	s_mov_b64 s[26:27], 0x6000
	s_add_i32 s3, s22, 0x4000
	s_mov_b32 m0, s3
	s_nop 0
	global_load_lds_dwordx4 v[108:109], off
	v_lshl_add_u64 v[106:107], v[104:105], 0, s[26:27]
	s_add_i32 s3, s22, 0x6000
	s_mov_b32 m0, s3
	s_nop 0
	global_load_lds_dwordx4 v[106:107], off
	v_lshl_add_u64 v[98:99], v[4:5], 0, v[96:97]
	s_mov_b32 m0, s24
	s_nop 0
	global_load_lds_dwordx4 v[98:99], off
	v_lshl_add_u64 v[100:101], v[98:99], 0, s[4:5]
	s_add_i32 s3, s22, 0xa000
	s_mov_b32 m0, s3
	s_nop 0
	global_load_lds_dwordx4 v[100:101], off
	v_lshl_add_u64 v[102:103], v[98:99], 0, s[6:7]
	s_add_i32 s3, s22, 0xc000
	s_mov_b32 m0, s3
	s_nop 0
	global_load_lds_dwordx4 v[102:103], off
	s_mov_b32 s21, 1
	s_mov_b32 s23, 0
	s_cmp_lt_i32 s10, 64
	v_mov_b32_e32 v96, v97
	v_mov_b32_e32 v95, v97
	v_mov_b32_e32 v94, v97
	v_mov_b32_e32 v93, v97
	v_mov_b32_e32 v92, v97
	v_mov_b32_e32 v91, v97
	v_mov_b32_e32 v90, v97
	v_mov_b32_e32 v89, v97
	v_mov_b32_e32 v88, v97
	v_mov_b32_e32 v87, v97
	v_mov_b32_e32 v86, v97
	v_mov_b32_e32 v85, v97
	v_mov_b32_e32 v84, v97
	v_mov_b32_e32 v83, v97
	v_mov_b32_e32 v82, v97
	v_mov_b32_e32 v81, v97
	v_mov_b32_e32 v80, v97
	v_mov_b32_e32 v79, v97
	v_mov_b32_e32 v78, v97
	v_mov_b32_e32 v77, v97
	v_mov_b32_e32 v76, v97
	v_mov_b32_e32 v75, v97
	v_mov_b32_e32 v74, v97
	v_mov_b32_e32 v73, v97
	v_mov_b32_e32 v72, v97
	v_mov_b32_e32 v71, v97
	v_mov_b32_e32 v70, v97
	v_mov_b32_e32 v69, v97
	v_mov_b32_e32 v68, v97
	v_mov_b32_e32 v67, v97
	v_mov_b32_e32 v66, v97
	v_mov_b32_e32 v65, v97
	v_mov_b32_e32 v64, v97
	v_mov_b32_e32 v63, v97
	v_mov_b32_e32 v62, v97
	v_mov_b32_e32 v61, v97
	v_mov_b32_e32 v60, v97
	v_mov_b32_e32 v59, v97
	v_mov_b32_e32 v58, v97
	v_mov_b32_e32 v57, v97
	v_mov_b32_e32 v56, v97
	v_mov_b32_e32 v55, v97
	v_mov_b32_e32 v54, v97
	v_mov_b32_e32 v53, v97
	v_mov_b32_e32 v52, v97
	v_mov_b32_e32 v51, v97
	v_mov_b32_e32 v50, v97
	v_mov_b32_e32 v49, v97
	v_mov_b32_e32 v48, v97
	v_mov_b32_e32 v47, v97
	v_mov_b32_e32 v46, v97
	v_mov_b32_e32 v45, v97
	v_mov_b32_e32 v44, v97
	v_mov_b32_e32 v43, v97
	v_mov_b32_e32 v42, v97
	v_mov_b32_e32 v41, v97
	v_mov_b32_e32 v40, v97
	v_mov_b32_e32 v39, v97
	v_mov_b32_e32 v38, v97
	v_mov_b32_e32 v37, v97
	v_mov_b32_e32 v36, v97
	v_mov_b32_e32 v35, v97
	v_mov_b32_e32 v34, v97
	v_mov_b32_e32 v33, v97
	v_mov_b32_e32 v32, v97
	v_mov_b32_e32 v31, v97
	v_mov_b32_e32 v30, v97
	v_mov_b32_e32 v29, v97
	v_mov_b32_e32 v28, v97
	v_mov_b32_e32 v27, v97
	v_mov_b32_e32 v26, v97
	v_mov_b32_e32 v25, v97
	v_mov_b32_e32 v24, v97
	v_mov_b32_e32 v23, v97
	v_mov_b32_e32 v22, v97
	v_mov_b32_e32 v21, v97
	v_mov_b32_e32 v20, v97
	v_mov_b32_e32 v19, v97
	v_mov_b32_e32 v18, v97
	v_mov_b32_e32 v17, v97
	v_mov_b32_e32 v16, v97
	v_mov_b32_e32 v15, v97
	v_mov_b32_e32 v14, v97
	v_mov_b32_e32 v13, v97
	v_mov_b32_e32 v12, v97
	v_mov_b32_e32 v11, v97
	v_mov_b32_e32 v10, v97
	v_mov_b32_e32 v9, v97
	v_mov_b32_e32 v8, v97
	v_mov_b32_e32 v7, v97
	v_mov_b32_e32 v6, v97
	v_mov_b32_e32 v5, v97
	v_mov_b32_e32 v4, v97
	v_mov_b32_e32 v3, v97
	v_mov_b32_e32 v2, v97
	v_and_b32_e32 v162, 31, v0
	v_bfe_u32 v1, v0, 5, 1
	s_cbranch_scc1 .LBB2_6
	s_ashr_i32 s3, s10, 31
	s_lshr_b32 s3, s3, 26
	s_add_i32 s3, s10, s3
	v_lshrrev_b32_e32 v2, 1, v0
	s_ashr_i32 s25, s3, 6
	v_bitop3_b32 v2, v1, v2, 7 bitop3:0x78
	s_cmp_lg_u32 0, -1
	v_lshlrev_b32_e32 v120, 4, v2
	v_or_b32_e32 v2, s20, v162
	s_cselect_b32 s3, 0, 0
	v_lshl_add_u32 v121, v2, 7, 0
	v_or_b32_e32 v2, s16, v162
	s_mov_b32 s10, s8
	s_add_i32 s8, s3, s2
	s_ashr_i32 s3, s9, 31
	s_mov_b32 s2, s9
	v_lshl_add_u32 v122, v2, 7, 0
	s_lshl_b64 s[2:3], s[2:3], 7
	v_mov_b32_e32 v2, 0
	s_addk_i32 s8, 0x6000
	v_xor_b32_e32 v123, 32, v120
	v_xor_b32_e32 v124, 64, v120
	v_xor_b32_e32 v125, 0x60, v120
	s_lshl_b64 s[4:5], s[10:11], 7
	s_mov_b64 s[6:7], s[2:3]
	s_mov_b32 s9, 0
	v_mov_b32_e32 v3, v2
	v_mov_b32_e32 v4, v2
	v_mov_b32_e32 v5, v2
	v_mov_b32_e32 v6, v2
	v_mov_b32_e32 v7, v2
	v_mov_b32_e32 v8, v2
	v_mov_b32_e32 v9, v2
	v_mov_b32_e32 v10, v2
	v_mov_b32_e32 v11, v2
	v_mov_b32_e32 v12, v2
	v_mov_b32_e32 v13, v2
	v_mov_b32_e32 v14, v2
	v_mov_b32_e32 v15, v2
	v_mov_b32_e32 v16, v2
	v_mov_b32_e32 v17, v2
	v_mov_b32_e32 v18, v2
	v_mov_b32_e32 v19, v2
	v_mov_b32_e32 v20, v2
	v_mov_b32_e32 v21, v2
	v_mov_b32_e32 v22, v2
	v_mov_b32_e32 v23, v2
	v_mov_b32_e32 v24, v2
	v_mov_b32_e32 v25, v2
	v_mov_b32_e32 v26, v2
	v_mov_b32_e32 v27, v2
	v_mov_b32_e32 v28, v2
	v_mov_b32_e32 v29, v2
	v_mov_b32_e32 v30, v2
	v_mov_b32_e32 v31, v2
	v_mov_b32_e32 v32, v2
	v_mov_b32_e32 v33, v2
	v_mov_b32_e32 v34, v2
	v_mov_b32_e32 v35, v2
	v_mov_b32_e32 v36, v2
	v_mov_b32_e32 v37, v2
	v_mov_b32_e32 v38, v2
	v_mov_b32_e32 v39, v2
	v_mov_b32_e32 v40, v2
	v_mov_b32_e32 v41, v2
	v_mov_b32_e32 v42, v2
	v_mov_b32_e32 v43, v2
	v_mov_b32_e32 v44, v2
	v_mov_b32_e32 v45, v2
	v_mov_b32_e32 v46, v2
	v_mov_b32_e32 v47, v2
	v_mov_b32_e32 v48, v2
	v_mov_b32_e32 v49, v2
	v_mov_b32_e32 v50, v2
	v_mov_b32_e32 v51, v2
	v_mov_b32_e32 v52, v2
	v_mov_b32_e32 v53, v2
	v_mov_b32_e32 v54, v2
	v_mov_b32_e32 v55, v2
	v_mov_b32_e32 v56, v2
	v_mov_b32_e32 v57, v2
	v_mov_b32_e32 v58, v2
	v_mov_b32_e32 v59, v2
	v_mov_b32_e32 v60, v2
	v_mov_b32_e32 v61, v2
	v_mov_b32_e32 v62, v2
	v_mov_b32_e32 v63, v2
	v_mov_b32_e32 v64, v2
	v_mov_b32_e32 v65, v2
	v_mov_b32_e32 v66, v2
	v_mov_b32_e32 v67, v2
	v_mov_b32_e32 v68, v2
	v_mov_b32_e32 v69, v2
	v_mov_b32_e32 v70, v2
	v_mov_b32_e32 v71, v2
	v_mov_b32_e32 v72, v2
	v_mov_b32_e32 v73, v2
	v_mov_b32_e32 v74, v2
	v_mov_b32_e32 v75, v2
	v_mov_b32_e32 v76, v2
	v_mov_b32_e32 v77, v2
	v_mov_b32_e32 v78, v2
	v_mov_b32_e32 v79, v2
	v_mov_b32_e32 v80, v2
	v_mov_b32_e32 v81, v2
	v_mov_b32_e32 v82, v2
	v_mov_b32_e32 v83, v2
	v_mov_b32_e32 v84, v2
	v_mov_b32_e32 v85, v2
	v_mov_b32_e32 v86, v2
	v_mov_b32_e32 v87, v2
	v_mov_b32_e32 v88, v2
	v_mov_b32_e32 v89, v2
	v_mov_b32_e32 v90, v2
	v_mov_b32_e32 v91, v2
	v_mov_b32_e32 v92, v2
	v_mov_b32_e32 v93, v2
	v_mov_b32_e32 v94, v2
	v_mov_b32_e32 v95, v2
	v_mov_b32_e32 v96, v2
	v_mov_b32_e32 v97, v2
	v_lshl_add_u64 v[168:169], v[104:105], 0, s[4:5]
	v_lshl_add_u64 v[170:171], v[110:111], 0, s[4:5]
	v_lshl_add_u64 v[172:173], v[108:109], 0, s[4:5]
	v_lshl_add_u64 v[174:175], v[106:107], 0, s[4:5]
	v_lshl_add_u64 v[176:177], v[98:99], 0, s[2:3]
	v_lshl_add_u64 v[178:179], v[100:101], 0, s[2:3]
	v_lshl_add_u64 v[180:181], v[102:103], 0, s[2:3]
	s_mov_b32 s9, 1
	s_add_i32 s25, s25, -1
	s_cmp_ge_u32 s14, 4
	s_cbranch_scc1 .Lqkv_a0
	s_setprio 1
	s_waitcnt vmcnt(0) lgkmcnt(0)
	s_barrier
	s_mul_i32 s10, s23, 0xe000
	s_mul_i32 s11, s21, 0xe000
	v_add_u32_e32 v142, s10, v122
	v_add_u32_e32 v143, s10, v121
	s_add_i32 s11, s11, s22
	s_xor_b32 s23, s23, 1
	s_xor_b32 s21, s21, 1
	v_add_u32_e32 v144, v142, v120
	v_add_u32_e32 v145, v143, v120
	ds_read_b128 v[130:133], v145
	ds_read_b128 v[104:107], v144 offset:32768
	ds_read_b128 v[108:111], v144 offset:36864
	ds_read_b128 v[134:137], v145 offset:4096
	ds_read_b128 v[126:129], v144 offset:40960
	s_mov_b32 m0, s11
	s_nop 0
	global_load_lds_dwordx4 v[168:169], off
	v_lshl_add_u64 v[168:169], v[168:169], 0, s[4:5]
	s_add_i32 m0, s11, 0x2000
	s_nop 0
	global_load_lds_dwordx4 v[170:171], off
	v_lshl_add_u64 v[170:171], v[170:171], 0, s[4:5]
	s_add_i32 m0, s11, 0x4000
	s_nop 0
	global_load_lds_dwordx4 v[172:173], off
	v_lshl_add_u64 v[172:173], v[172:173], 0, s[4:5]
	v_add_u32_e32 v146, v142, v123
	v_add_u32_e32 v147, v143, v123
	ds_read_b128 v[182:185], v147
	ds_read_b128 v[138:141], v146 offset:32768
	ds_read_b128 v[112:115], v146 offset:36864
	ds_read_b128 v[186:189], v147 offset:4096
	ds_read_b128 v[116:119], v146 offset:40960
	s_waitcnt lgkmcnt(8)
	s_add_i32 m0, s11, 0x6000
	v_mfma_f32_32x32x16_f16 v[82:97], v[104:107], v[130:133], v[82:97]
	global_load_lds_dwordx4 v[174:175], off
	v_lshl_add_u64 v[174:175], v[174:175], 0, s[4:5]
	s_waitcnt lgkmcnt(7)
	v_mfma_f32_32x32x16_f16 v[66:81], v[108:111], v[130:133], v[66:81]
	s_waitcnt lgkmcnt(6)
	s_add_i32 m0, s11, 0x8000
	v_mfma_f32_32x32x16_f16 v[34:49], v[104:107], v[134:137], v[34:49]
	global_load_lds_dwordx4 v[176:177], off
	v_lshl_add_u64 v[176:177], v[176:177], 0, s[2:3]
	v_mfma_f32_32x32x16_f16 v[18:33], v[108:111], v[134:137], v[18:33]
	s_waitcnt lgkmcnt(5)
	s_add_i32 m0, s11, 0xa000
	v_mfma_f32_32x32x16_f16 v[50:65], v[126:129], v[130:133], v[50:65]
	global_load_lds_dwordx4 v[178:179], off
	v_lshl_add_u64 v[178:179], v[178:179], 0, s[2:3]
	v_mfma_f32_32x32x16_f16 v[2:17], v[126:129], v[134:137], v[2:17]
	v_add_u32_e32 v144, v142, v124
	v_add_u32_e32 v145, v143, v124
	ds_read_b128 v[130:133], v145
	ds_read_b128 v[104:107], v144 offset:32768
	ds_read_b128 v[108:111], v144 offset:36864
	ds_read_b128 v[134:137], v145 offset:4096
	ds_read_b128 v[126:129], v144 offset:40960
	s_waitcnt lgkmcnt(8)
	s_add_i32 m0, s11, 0xc000
	v_mfma_f32_32x32x16_f16 v[82:97], v[138:141], v[182:185], v[82:97]
	global_load_lds_dwordx4 v[180:181], off
	v_lshl_add_u64 v[180:181], v[180:181], 0, s[2:3]
	s_waitcnt lgkmcnt(7)
	v_mfma_f32_32x32x16_f16 v[66:81], v[112:115], v[182:185], v[66:81]
	s_waitcnt lgkmcnt(6)
	v_mfma_f32_32x32x16_f16 v[34:49], v[138:141], v[186:189], v[34:49]
	v_mfma_f32_32x32x16_f16 v[18:33], v[112:115], v[186:189], v[18:33]
	s_waitcnt lgkmcnt(5)
	v_mfma_f32_32x32x16_f16 v[50:65], v[116:119], v[182:185], v[50:65]
	v_mfma_f32_32x32x16_f16 v[2:17], v[116:119], v[186:189], v[2:17]
	v_add_u32_e32 v146, v142, v125
	v_add_u32_e32 v147, v143, v125
	ds_read_b128 v[182:185], v147
	ds_read_b128 v[138:141], v146 offset:32768
	ds_read_b128 v[112:115], v146 offset:36864
	ds_read_b128 v[186:189], v147 offset:4096
	ds_read_b128 v[116:119], v146 offset:40960
	s_waitcnt lgkmcnt(8)
	v_mfma_f32_32x32x16_f16 v[82:97], v[104:107], v[130:133], v[82:97]
	s_waitcnt lgkmcnt(7)
	v_mfma_f32_32x32x16_f16 v[66:81], v[108:111], v[130:133], v[66:81]
	s_waitcnt lgkmcnt(6)
	v_mfma_f32_32x32x16_f16 v[34:49], v[104:107], v[134:137], v[34:49]
	v_mfma_f32_32x32x16_f16 v[18:33], v[108:111], v[134:137], v[18:33]
	s_waitcnt lgkmcnt(5)
	v_mfma_f32_32x32x16_f16 v[50:65], v[126:129], v[130:133], v[50:65]
	v_mfma_f32_32x32x16_f16 v[2:17], v[126:129], v[134:137], v[2:17]
.Lqkv_loop:
	s_waitcnt vmcnt(0) lgkmcnt(0)
	s_barrier
	s_mul_i32 s10, s23, 0xe000
	s_mul_i32 s11, s21, 0xe000
	v_add_u32_e32 v142, s10, v122
	v_add_u32_e32 v143, s10, v121
	s_add_i32 s11, s11, s22
	s_xor_b32 s23, s23, 1
	s_xor_b32 s21, s21, 1
	v_add_u32_e32 v144, v142, v120
	v_add_u32_e32 v145, v143, v120
	ds_read_b128 v[130:133], v145
	ds_read_b128 v[104:107], v144 offset:32768
	ds_read_b128 v[108:111], v144 offset:36864
	ds_read_b128 v[134:137], v145 offset:4096
	ds_read_b128 v[126:129], v144 offset:40960
	s_mov_b32 m0, s11
	v_mfma_f32_32x32x16_f16 v[82:97], v[138:141], v[182:185], v[82:97]
	global_load_lds_dwordx4 v[168:169], off
	v_lshl_add_u64 v[168:169], v[168:169], 0, s[4:5]
	v_mfma_f32_32x32x16_f16 v[66:81], v[112:115], v[182:185], v[66:81]
	s_add_i32 m0, s11, 0x2000
	v_mfma_f32_32x32x16_f16 v[34:49], v[138:141], v[186:189], v[34:49]
	global_load_lds_dwordx4 v[170:171], off
	v_lshl_add_u64 v[170:171], v[170:171], 0, s[4:5]
	v_mfma_f32_32x32x16_f16 v[18:33], v[112:115], v[186:189], v[18:33]
	s_add_i32 m0, s11, 0x4000
	v_mfma_f32_32x32x16_f16 v[50:65], v[116:119], v[182:185], v[50:65]
	global_load_lds_dwordx4 v[172:173], off
	v_lshl_add_u64 v[172:173], v[172:173], 0, s[4:5]
	v_mfma_f32_32x32x16_f16 v[2:17], v[116:119], v[186:189], v[2:17]
	v_add_u32_e32 v146, v142, v123
	v_add_u32_e32 v147, v143, v123
	ds_read_b128 v[182:185], v147
	ds_read_b128 v[138:141], v146 offset:32768
	ds_read_b128 v[112:115], v146 offset:36864
	ds_read_b128 v[186:189], v147 offset:4096
	ds_read_b128 v[116:119], v146 offset:40960
	s_waitcnt lgkmcnt(8)
	s_add_i32 m0, s11, 0x6000
	v_mfma_f32_32x32x16_f16 v[82:97], v[104:107], v[130:133], v[82:97]
	global_load_lds_dwordx4 v[174:175], off
	v_lshl_add_u64 v[174:175], v[174:175], 0, s[4:5]
	s_waitcnt lgkmcnt(7)
	v_mfma_f32_32x32x16_f16 v[66:81], v[108:111], v[130:133], v[66:81]
	s_waitcnt lgkmcnt(6)
	s_add_i32 m0, s11, 0x8000
	v_mfma_f32_32x32x16_f16 v[34:49], v[104:107], v[134:137], v[34:49]
	global_load_lds_dwordx4 v[176:177], off
	v_lshl_add_u64 v[176:177], v[176:177], 0, s[2:3]
	v_mfma_f32_32x32x16_f16 v[18:33], v[108:111], v[134:137], v[18:33]
	s_waitcnt lgkmcnt(5)
	s_add_i32 m0, s11, 0xa000
	v_mfma_f32_32x32x16_f16 v[50:65], v[126:129], v[130:133], v[50:65]
	global_load_lds_dwordx4 v[178:179], off
	v_lshl_add_u64 v[178:179], v[178:179], 0, s[2:3]
	v_mfma_f32_32x32x16_f16 v[2:17], v[126:129], v[134:137], v[2:17]
	v_add_u32_e32 v144, v142, v124
	v_add_u32_e32 v145, v143, v124
	ds_read_b128 v[130:133], v145
	ds_read_b128 v[104:107], v144 offset:32768
	ds_read_b128 v[108:111], v144 offset:36864
	ds_read_b128 v[134:137], v145 offset:4096
	ds_read_b128 v[126:129], v144 offset:40960
	s_waitcnt lgkmcnt(8)
	s_add_i32 m0, s11, 0xc000
	v_mfma_f32_32x32x16_f16 v[82:97], v[138:141], v[182:185], v[82:97]
	global_load_lds_dwordx4 v[180:181], off
	v_lshl_add_u64 v[180:181], v[180:181], 0, s[2:3]
	s_waitcnt lgkmcnt(7)
	v_mfma_f32_32x32x16_f16 v[66:81], v[112:115], v[182:185], v[66:81]
	s_waitcnt lgkmcnt(6)
	v_mfma_f32_32x32x16_f16 v[34:49], v[138:141], v[186:189], v[34:49]
	v_mfma_f32_32x32x16_f16 v[18:33], v[112:115], v[186:189], v[18:33]
	s_waitcnt lgkmcnt(5)
	v_mfma_f32_32x32x16_f16 v[50:65], v[116:119], v[182:185], v[50:65]
	v_mfma_f32_32x32x16_f16 v[2:17], v[116:119], v[186:189], v[2:17]
	v_add_u32_e32 v146, v142, v125
	v_add_u32_e32 v147, v143, v125
	ds_read_b128 v[182:185], v147
	ds_read_b128 v[138:141], v146 offset:32768
	ds_read_b128 v[112:115], v146 offset:36864
	ds_read_b128 v[186:189], v147 offset:4096
	ds_read_b128 v[116:119], v146 offset:40960
	s_waitcnt lgkmcnt(8)
	v_mfma_f32_32x32x16_f16 v[82:97], v[104:107], v[130:133], v[82:97]
	s_waitcnt lgkmcnt(7)
	v_mfma_f32_32x32x16_f16 v[66:81], v[108:111], v[130:133], v[66:81]
	s_waitcnt lgkmcnt(6)
	v_mfma_f32_32x32x16_f16 v[34:49], v[104:107], v[134:137], v[34:49]
	v_mfma_f32_32x32x16_f16 v[18:33], v[108:111], v[134:137], v[18:33]
	s_waitcnt lgkmcnt(5)
	v_mfma_f32_32x32x16_f16 v[50:65], v[126:129], v[130:133], v[50:65]
	v_mfma_f32_32x32x16_f16 v[2:17], v[126:129], v[134:137], v[2:17]
	s_add_i32 s9, s9, 1
	s_cmp_lt_i32 s9, s25
	s_cbranch_scc1 .Lqkv_loop
	s_waitcnt vmcnt(0) lgkmcnt(0)
	s_barrier
	s_mul_i32 s10, s23, 0xe000
	v_add_u32_e32 v142, s10, v122
	v_add_u32_e32 v143, s10, v121
	s_xor_b32 s23, s23, 1
	s_xor_b32 s21, s21, 1
	v_add_u32_e32 v144, v142, v120
	v_add_u32_e32 v145, v143, v120
	ds_read_b128 v[130:133], v145
	ds_read_b128 v[104:107], v144 offset:32768
	ds_read_b128 v[108:111], v144 offset:36864
	ds_read_b128 v[134:137], v145 offset:4096
	ds_read_b128 v[126:129], v144 offset:40960
	v_mfma_f32_32x32x16_f16 v[82:97], v[138:141], v[182:185], v[82:97]
	v_mfma_f32_32x32x16_f16 v[66:81], v[112:115], v[182:185], v[66:81]
	v_mfma_f32_32x32x16_f16 v[34:49], v[138:141], v[186:189], v[34:49]
	v_mfma_f32_32x32x16_f16 v[18:33], v[112:115], v[186:189], v[18:33]
	v_mfma_f32_32x32x16_f16 v[50:65], v[116:119], v[182:185], v[50:65]
	v_mfma_f32_32x32x16_f16 v[2:17], v[116:119], v[186:189], v[2:17]
	v_add_u32_e32 v146, v142, v123
	v_add_u32_e32 v147, v143, v123
	ds_read_b128 v[182:185], v147
	ds_read_b128 v[138:141], v146 offset:32768
	ds_read_b128 v[112:115], v146 offset:36864
	ds_read_b128 v[186:189], v147 offset:4096
	ds_read_b128 v[116:119], v146 offset:40960
	s_waitcnt lgkmcnt(8)
	v_mfma_f32_32x32x16_f16 v[82:97], v[104:107], v[130:133], v[82:97]
	s_waitcnt lgkmcnt(7)
	v_mfma_f32_32x32x16_f16 v[66:81], v[108:111], v[130:133], v[66:81]
	s_waitcnt lgkmcnt(6)
	v_mfma_f32_32x32x16_f16 v[34:49], v[104:107], v[134:137], v[34:49]
	v_mfma_f32_32x32x16_f16 v[18:33], v[108:111], v[134:137], v[18:33]
	s_waitcnt lgkmcnt(5)
	v_mfma_f32_32x32x16_f16 v[50:65], v[126:129], v[130:133], v[50:65]
	v_mfma_f32_32x32x16_f16 v[2:17], v[126:129], v[134:137], v[2:17]
	v_add_u32_e32 v144, v142, v124
	v_add_u32_e32 v145, v143, v124
	ds_read_b128 v[130:133], v145
	ds_read_b128 v[104:107], v144 offset:32768
	ds_read_b128 v[108:111], v144 offset:36864
	ds_read_b128 v[134:137], v145 offset:4096
	ds_read_b128 v[126:129], v144 offset:40960
	s_waitcnt lgkmcnt(8)
	v_mfma_f32_32x32x16_f16 v[82:97], v[138:141], v[182:185], v[82:97]
	s_waitcnt lgkmcnt(7)
	v_mfma_f32_32x32x16_f16 v[66:81], v[112:115], v[182:185], v[66:81]
	s_waitcnt lgkmcnt(6)
	v_mfma_f32_32x32x16_f16 v[34:49], v[138:141], v[186:189], v[34:49]
	v_mfma_f32_32x32x16_f16 v[18:33], v[112:115], v[186:189], v[18:33]
	s_waitcnt lgkmcnt(5)
	v_mfma_f32_32x32x16_f16 v[50:65], v[116:119], v[182:185], v[50:65]
	v_mfma_f32_32x32x16_f16 v[2:17], v[116:119], v[186:189], v[2:17]
	v_add_u32_e32 v146, v142, v125
	v_add_u32_e32 v147, v143, v125
	ds_read_b128 v[182:185], v147
	ds_read_b128 v[138:141], v146 offset:32768
	ds_read_b128 v[112:115], v146 offset:36864
	ds_read_b128 v[186:189], v147 offset:4096
	ds_read_b128 v[116:119], v146 offset:40960
	s_waitcnt lgkmcnt(8)
	v_mfma_f32_32x32x16_f16 v[82:97], v[104:107], v[130:133], v[82:97]
	s_waitcnt lgkmcnt(7)
	v_mfma_f32_32x32x16_f16 v[66:81], v[108:111], v[130:133], v[66:81]
	s_waitcnt lgkmcnt(6)
	v_mfma_f32_32x32x16_f16 v[34:49], v[104:107], v[134:137], v[34:49]
	v_mfma_f32_32x32x16_f16 v[18:33], v[108:111], v[134:137], v[18:33]
	s_waitcnt lgkmcnt(5)
	v_mfma_f32_32x32x16_f16 v[50:65], v[126:129], v[130:133], v[50:65]
	v_mfma_f32_32x32x16_f16 v[2:17], v[126:129], v[134:137], v[2:17]
	s_waitcnt lgkmcnt(0)
	v_mfma_f32_32x32x16_f16 v[82:97], v[138:141], v[182:185], v[82:97]
	v_mfma_f32_32x32x16_f16 v[66:81], v[112:115], v[182:185], v[66:81]
	v_mfma_f32_32x32x16_f16 v[34:49], v[138:141], v[186:189], v[34:49]
	v_mfma_f32_32x32x16_f16 v[18:33], v[112:115], v[186:189], v[18:33]
	v_mfma_f32_32x32x16_f16 v[50:65], v[116:119], v[182:185], v[50:65]
	v_mfma_f32_32x32x16_f16 v[2:17], v[116:119], v[186:189], v[2:17]
	s_setprio 0
	s_branch .LBB2_6
